# speedup vs baseline: 1.0373x; 1.0023x over previous
_Z12fused_kernel6Params:
	s_load_dwordx16 s[52:67], s[0:1], 0x0
	s_load_dwordx16 s[36:51], s[0:1], 0x40
	s_load_dwordx16 s[8:23], s[0:1], 0x80
	s_load_dwordx4 s[24:27], s[0:1], 0xc0
	s_and_b32 s3, s2, 0x7f
	s_cmpk_gt_u32 s2, 0x7f
	v_and_b32_e32 v80, 63, v0
	s_mov_b64 s[0:1], -1
	s_mul_i32 s33, s3, 0x1c20
	s_cbranch_scc0 .Lk_217
	s_sleep 64
	v_readfirstlane_b32 s4, v0
	s_cmpk_lt_u32 s4, 0x300
	s_cbranch_scc1 .Lk_3
	s_setprio 1

.Lk_144:
	v_or_b32_e32 v46, 0x400, v54
	buffer_load_dwordx4 v[46:49], v46, s[4:7], 0 offen sc1
	ds_read_b128 v[50:53], v1
	v_mov_b32_e32 v66, 0
	v_add_u32_e32 v63, 0x800, v54
	s_mov_b32 s9, 0
	v_mov_b32_e32 v67, 0
	v_mov_b32_e32 v68, 0
	v_mov_b32_e32 v62, 0xc038aa3b
	s_mov_b32 s8, 0x4038aa3b
	v_mov_b32_e32 v65, 0
	v_mov_b32_e32 v64, v66
	s_setprio 2
	v_mov_b32_e32 v92, 0xc038aa3b
	v_mov_b32_e32 v93, 0xc038aa3b
	s_mov_b32 s8, 0x4038aa3b
	s_mov_b32 s9, 0
	v_mov_b32_e32 v64, 0
	v_mov_b32_e32 v65, 0
	v_mov_b32_e32 v66, 0
	v_mov_b32_e32 v67, 0
	v_mov_b32_e32 v68, 0
	v_mov_b32_e32 v116, v1
	v_mov_b32_e32 v117, v63
	s_mov_b32 s12, 0
	s_waitcnt lgkmcnt(0)
	v_mfma_f32_16x16x32_f16 v[84:87], v[6:9], v[50:53], v[18:21]
	v_mfma_f32_16x16x32_f16 v[88:91], v[10:13], v[50:53], v[38:41]
	ds_read_b128 v[56:59], v75 offset:2048
	ds_read_b128 v[60:63], v75 offset:3072
	s_waitcnt vmcnt(1)
	v_mfma_f32_16x16x32_f16 v[84:87], v[2:5], v[42:45], v[84:87]
	v_mfma_f32_16x16x32_f16 v[88:91], v[14:17], v[42:45], v[88:91]
	v_readfirstlane_b32 s10, v67
	v_readfirstlane_b32 s11, v68
	global_load_dword v67, v66, s[0:1] sc1
	global_load_dword v68, v66, s[0:1] offset:4 sc1
	s_min_u32 s10, s10, s11
	s_max_u32 s14, s14, s10
	s_waitcnt lgkmcnt(1)
	v_mfma_f32_16x16x32_f16 v[84:87], v[30:33], v[56:59], v[84:87]
	v_mfma_f32_16x16x32_f16 v[88:91], v[22:25], v[56:59], v[88:91]
	s_waitcnt lgkmcnt(0)
	v_mfma_f32_16x16x32_f16 v[84:87], v[34:37], v[60:63], v[84:87]
	v_mfma_f32_16x16x32_f16 v[88:91], v[26:29], v[60:63], v[88:91]
	s_add_u32 s13, s12, 3
	s_min_u32 s13, s13, 450
	s_cmp_ge_u32 s14, s13
	s_cbranch_scc1 .Lca_ok_1
	s_mov_b32 s15, 0

.Lca_ok_1:
	buffer_load_dwordx4 v[42:45], v117, s[4:7], 0 offen offset:0 sc1
	ds_read_b128 v[50:53], v116 offset:256
	s_nop 1
	v_exp_f32_e32 v94, v86
	v_exp_f32_e32 v95, v90
	v_exp_f32_e32 v96, v84
	v_exp_f32_e32 v97, v88
	v_exp_f32_e32 v98, v85
	v_exp_f32_e32 v99, v89
	v_pk_add_f32 v[100:101], v[94:95], 1.0 op_sel_hi:[1,0]
	v_pk_fma_f32 v[102:103], v[94:95], s[8:9], v[92:93] op_sel_hi:[1,0,0]
	v_pk_fma_f32 v[100:101], v[96:97], v[100:101], v[100:101]
	v_pk_fma_f32 v[104:105], v[100:101], v[98:99], v[100:101]
	v_rcp_f32_e32 v104, v104
	v_rcp_f32_e32 v105, v105
	v_pk_fma_f32 v[102:103], v[102:103], v[98:99], v[102:103]
	v_pk_fma_f32 v[102:103], v[64:65], v[100:101], v[102:103]
	v_exp_f32_e32 v106, v87
	v_pk_mul_f32 v[64:65], v[102:103], v[104:105]
	v_exp_f32_e32 v108, v64
	v_exp_f32_e32 v109, v65
	v_exp_f32_e32 v107, v91
	v_pk_add_f32 v[110:111], v[108:109], 1.0 op_sel_hi:[1,0]
	v_pk_fma_f32 v[110:111], v[110:111], v[106:107], v[110:111]
	v_rcp_f32_e32 v110, v110
	v_rcp_f32_e32 v111, v111
	v_pk_add_f32 v[112:113], v[108:109], -1.0 op_sel_hi:[1,0]
	v_pk_mul_f32 v[112:113], v[112:113], v[110:111]
	v_cvt_pk_f16_f32 v114, v112, v113
	ds_write_b32 v81, v114 offset:0
	s_waitcnt lgkmcnt(0)
	s_barrier
	v_mfma_f32_16x16x32_f16 v[84:87], v[6:9], v[50:53], v[18:21]
	v_mfma_f32_16x16x32_f16 v[88:91], v[10:13], v[50:53], v[38:41]
	ds_read_b128 v[56:59], v75 offset:0
	ds_read_b128 v[60:63], v75 offset:1024
	s_waitcnt vmcnt(3)
	v_mfma_f32_16x16x32_f16 v[84:87], v[2:5], v[46:49], v[84:87]
	v_mfma_f32_16x16x32_f16 v[88:91], v[14:17], v[46:49], v[88:91]
	s_waitcnt lgkmcnt(1)
	v_mfma_f32_16x16x32_f16 v[84:87], v[30:33], v[56:59], v[84:87]
	v_mfma_f32_16x16x32_f16 v[88:91], v[22:25], v[56:59], v[88:91]
	s_waitcnt lgkmcnt(0)
	v_mfma_f32_16x16x32_f16 v[84:87], v[34:37], v[60:63], v[84:87]
	v_mfma_f32_16x16x32_f16 v[88:91], v[26:29], v[60:63], v[88:91]
	s_add_u32 s13, s12, 4
	s_min_u32 s13, s13, 450
	s_cmp_ge_u32 s14, s13
	s_cbranch_scc1 .Lca_ok_3
	s_mov_b32 s15, 0

.Lca_loop:
	s_barrier
	v_mfma_f32_16x16x32_f16 v[84:87], v[6:9], v[50:53], v[18:21]
	v_mfma_f32_16x16x32_f16 v[88:91], v[10:13], v[50:53], v[38:41]
	ds_read_b128 v[56:59], v75 offset:2048
	ds_read_b128 v[60:63], v75 offset:3072
	s_waitcnt vmcnt(1)
	v_mfma_f32_16x16x32_f16 v[84:87], v[2:5], v[42:45], v[84:87]
	v_mfma_f32_16x16x32_f16 v[88:91], v[14:17], v[42:45], v[88:91]
	v_readfirstlane_b32 s10, v67
	v_readfirstlane_b32 s11, v68
	global_load_dword v67, v66, s[0:1] sc1
	global_load_dword v68, v66, s[0:1] offset:4 sc1
	s_min_u32 s10, s10, s11
	s_max_u32 s14, s14, s10
	s_waitcnt lgkmcnt(1)
	v_mfma_f32_16x16x32_f16 v[84:87], v[30:33], v[56:59], v[84:87]
	v_mfma_f32_16x16x32_f16 v[88:91], v[22:25], v[56:59], v[88:91]
	s_waitcnt lgkmcnt(0)
	v_mfma_f32_16x16x32_f16 v[84:87], v[34:37], v[60:63], v[84:87]
	v_mfma_f32_16x16x32_f16 v[88:91], v[26:29], v[60:63], v[88:91]
	s_add_u32 s13, s12, 3
	s_min_u32 s13, s13, 450
	s_cmp_ge_u32 s14, s13
	s_cbranch_scc1 .Lca_ok_5
	s_mov_b32 s15, 0

.Lca_ok_5:
	buffer_load_dwordx4 v[42:45], v117, s[4:7], 0 offen offset:0 sc1
	ds_read_b128 v[50:53], v116 offset:256
	s_nop 1
	v_min_f32_e32 v64, 0x42700000, v64
	v_min_f32_e32 v65, 0x42700000, v65
	v_exp_f32_e32 v94, v86
	v_exp_f32_e32 v95, v90
	v_exp_f32_e32 v96, v84
	v_exp_f32_e32 v97, v88
	v_exp_f32_e32 v98, v85
	v_exp_f32_e32 v99, v89
	v_pk_add_f32 v[100:101], v[94:95], 1.0 op_sel_hi:[1,0]
	v_pk_fma_f32 v[102:103], v[94:95], s[8:9], v[92:93] op_sel_hi:[1,0,0]
	v_pk_fma_f32 v[100:101], v[96:97], v[100:101], v[100:101]
	v_pk_fma_f32 v[104:105], v[100:101], v[98:99], v[100:101]
	v_rcp_f32_e32 v104, v104
	v_rcp_f32_e32 v105, v105
	v_pk_fma_f32 v[102:103], v[102:103], v[98:99], v[102:103]
	v_pk_fma_f32 v[102:103], v[64:65], v[100:101], v[102:103]
	v_exp_f32_e32 v106, v87
	v_pk_mul_f32 v[64:65], v[102:103], v[104:105]
	v_exp_f32_e32 v108, v64
	v_exp_f32_e32 v109, v65
	v_exp_f32_e32 v107, v91
	v_pk_add_f32 v[110:111], v[108:109], 1.0 op_sel_hi:[1,0]
	v_pk_fma_f32 v[110:111], v[110:111], v[106:107], v[110:111]
	v_rcp_f32_e32 v110, v110
	v_rcp_f32_e32 v111, v111
	v_pk_add_f32 v[112:113], v[108:109], -1.0 op_sel_hi:[1,0]
	v_pk_mul_f32 v[112:113], v[112:113], v[110:111]
	v_cvt_pk_f16_f32 v114, v112, v113
	ds_write_b32 v81, v114 offset:0
	s_waitcnt lgkmcnt(0)
	s_barrier
	v_mfma_f32_16x16x32_f16 v[84:87], v[6:9], v[50:53], v[18:21]
	v_mfma_f32_16x16x32_f16 v[88:91], v[10:13], v[50:53], v[38:41]
	ds_read_b128 v[56:59], v75 offset:0
	ds_read_b128 v[60:63], v75 offset:1024
	s_waitcnt vmcnt(3)
	v_mfma_f32_16x16x32_f16 v[84:87], v[2:5], v[46:49], v[84:87]
	v_mfma_f32_16x16x32_f16 v[88:91], v[14:17], v[46:49], v[88:91]
	s_waitcnt lgkmcnt(1)
	v_mfma_f32_16x16x32_f16 v[84:87], v[30:33], v[56:59], v[84:87]
	v_mfma_f32_16x16x32_f16 v[88:91], v[22:25], v[56:59], v[88:91]
	s_waitcnt lgkmcnt(0)
	v_mfma_f32_16x16x32_f16 v[84:87], v[34:37], v[60:63], v[84:87]
	v_mfma_f32_16x16x32_f16 v[88:91], v[26:29], v[60:63], v[88:91]
	s_add_u32 s13, s12, 4
	s_min_u32 s13, s13, 450
	s_cmp_ge_u32 s14, s13
	s_cbranch_scc1 .Lca_ok_7
	s_mov_b32 s15, 0

.Lca_ok_7:
	buffer_load_dwordx4 v[46:49], v117, s[4:7], 0 offen offset:1024 sc1
	ds_read_b128 v[50:53], v116 offset:512
	s_nop 1
	v_exp_f32_e32 v94, v86
	v_exp_f32_e32 v95, v90
	v_exp_f32_e32 v96, v84
	v_exp_f32_e32 v97, v88
	v_exp_f32_e32 v98, v85
	v_exp_f32_e32 v99, v89
	v_pk_add_f32 v[100:101], v[94:95], 1.0 op_sel_hi:[1,0]
	v_pk_fma_f32 v[102:103], v[94:95], s[8:9], v[92:93] op_sel_hi:[1,0,0]
	v_pk_fma_f32 v[100:101], v[96:97], v[100:101], v[100:101]
	v_pk_fma_f32 v[104:105], v[100:101], v[98:99], v[100:101]
	v_rcp_f32_e32 v104, v104
	v_rcp_f32_e32 v105, v105
	v_pk_fma_f32 v[102:103], v[102:103], v[98:99], v[102:103]
	v_pk_fma_f32 v[102:103], v[64:65], v[100:101], v[102:103]
	v_exp_f32_e32 v106, v87
	v_pk_mul_f32 v[64:65], v[102:103], v[104:105]
	v_exp_f32_e32 v108, v64
	v_exp_f32_e32 v109, v65
	v_exp_f32_e32 v107, v91
	v_pk_add_f32 v[110:111], v[108:109], 1.0 op_sel_hi:[1,0]
	v_pk_fma_f32 v[110:111], v[110:111], v[106:107], v[110:111]
	v_rcp_f32_e32 v110, v110
	v_rcp_f32_e32 v111, v111
	v_pk_add_f32 v[112:113], v[108:109], -1.0 op_sel_hi:[1,0]
	v_pk_mul_f32 v[112:113], v[112:113], v[110:111]
	v_cvt_pk_f16_f32 v114, v112, v113
	ds_write_b32 v81, v114 offset:2048
	s_waitcnt lgkmcnt(0)
	s_barrier
	v_mfma_f32_16x16x32_f16 v[84:87], v[6:9], v[50:53], v[18:21]
	v_mfma_f32_16x16x32_f16 v[88:91], v[10:13], v[50:53], v[38:41]
	ds_read_b128 v[56:59], v75 offset:2048
	ds_read_b128 v[60:63], v75 offset:3072
	s_waitcnt vmcnt(1)
	v_mfma_f32_16x16x32_f16 v[84:87], v[2:5], v[42:45], v[84:87]
	v_mfma_f32_16x16x32_f16 v[88:91], v[14:17], v[42:45], v[88:91]
	v_readfirstlane_b32 s10, v67
	v_readfirstlane_b32 s11, v68
	global_load_dword v67, v66, s[0:1] sc1
	global_load_dword v68, v66, s[0:1] offset:4 sc1
	s_min_u32 s10, s10, s11
	s_max_u32 s14, s14, s10
	s_waitcnt lgkmcnt(1)
	v_mfma_f32_16x16x32_f16 v[84:87], v[30:33], v[56:59], v[84:87]
	v_mfma_f32_16x16x32_f16 v[88:91], v[22:25], v[56:59], v[88:91]
	s_waitcnt lgkmcnt(0)
	v_mfma_f32_16x16x32_f16 v[84:87], v[34:37], v[60:63], v[84:87]
	v_mfma_f32_16x16x32_f16 v[88:91], v[26:29], v[60:63], v[88:91]
	s_add_u32 s13, s12, 5
	s_min_u32 s13, s13, 450
	s_cmp_ge_u32 s14, s13
	s_cbranch_scc1 .Lca_ok_9
	s_mov_b32 s15, 0

.Lca_ok_9:
	buffer_load_dwordx4 v[42:45], v117, s[4:7], 0 offen offset:2048 sc1
	ds_read_b128 v[50:53], v116 offset:768
	s_nop 1
	v_exp_f32_e32 v94, v86
	v_exp_f32_e32 v95, v90
	v_exp_f32_e32 v96, v84
	v_exp_f32_e32 v97, v88
	v_exp_f32_e32 v98, v85
	v_exp_f32_e32 v99, v89
	v_pk_add_f32 v[100:101], v[94:95], 1.0 op_sel_hi:[1,0]
	v_pk_fma_f32 v[102:103], v[94:95], s[8:9], v[92:93] op_sel_hi:[1,0,0]
	v_pk_fma_f32 v[100:101], v[96:97], v[100:101], v[100:101]
	v_pk_fma_f32 v[104:105], v[100:101], v[98:99], v[100:101]
	v_rcp_f32_e32 v104, v104
	v_rcp_f32_e32 v105, v105
	v_pk_fma_f32 v[102:103], v[102:103], v[98:99], v[102:103]
	v_pk_fma_f32 v[102:103], v[64:65], v[100:101], v[102:103]
	v_exp_f32_e32 v106, v87
	v_pk_mul_f32 v[64:65], v[102:103], v[104:105]
	v_exp_f32_e32 v108, v64
	v_exp_f32_e32 v109, v65
	v_exp_f32_e32 v107, v91
	v_pk_add_f32 v[110:111], v[108:109], 1.0 op_sel_hi:[1,0]
	v_pk_fma_f32 v[110:111], v[110:111], v[106:107], v[110:111]
	v_rcp_f32_e32 v110, v110
	v_rcp_f32_e32 v111, v111
	v_pk_add_f32 v[112:113], v[108:109], -1.0 op_sel_hi:[1,0]
	v_pk_mul_f32 v[112:113], v[112:113], v[110:111]
	v_cvt_pk_f16_f32 v114, v112, v113
	ds_write_b32 v81, v114 offset:0
	s_waitcnt lgkmcnt(0)
	s_barrier
	v_mfma_f32_16x16x32_f16 v[84:87], v[6:9], v[50:53], v[18:21]
	v_mfma_f32_16x16x32_f16 v[88:91], v[10:13], v[50:53], v[38:41]
	ds_read_b128 v[56:59], v75 offset:0
	ds_read_b128 v[60:63], v75 offset:1024
	s_waitcnt vmcnt(3)
	v_mfma_f32_16x16x32_f16 v[84:87], v[2:5], v[46:49], v[84:87]
	v_mfma_f32_16x16x32_f16 v[88:91], v[14:17], v[46:49], v[88:91]
	s_waitcnt lgkmcnt(1)
	v_mfma_f32_16x16x32_f16 v[84:87], v[30:33], v[56:59], v[84:87]
	v_mfma_f32_16x16x32_f16 v[88:91], v[22:25], v[56:59], v[88:91]
	s_waitcnt lgkmcnt(0)
	v_mfma_f32_16x16x32_f16 v[84:87], v[34:37], v[60:63], v[84:87]
	v_mfma_f32_16x16x32_f16 v[88:91], v[26:29], v[60:63], v[88:91]
	s_add_u32 s13, s12, 6
	s_min_u32 s13, s13, 450
	s_cmp_ge_u32 s14, s13
	s_cbranch_scc1 .Lca_ok_11
	s_mov_b32 s15, 0
